# s9 + OUT epilogues: residual loads of row groups 2..7 issued before waiting on group 1 (first HBM round trip covered)
# speedup vs baseline: 1.0046x; 1.0046x over previous
; template <int M> __device__ __forceinline__ float swz_xor(float v) { return __int_as_float(__builtin_amdgcn_ds_swizzle(__float_as_int(v), (M << 10) | 0x1f)); }
; __device__ __forceinline__ float half_sum(float v) { auto rr = __builtin_amdgcn_permlane32_swap(__float_as_uint(v), __float_as_uint(v), false, false); return __uint_as_float(rr[0]) + __uint_as_float(rr[1]); }
;     __device__ __forceinline__ bool run(const f32x4 (&v)[2][2][4][2], const Unit& u, int wr, int wc, int fr, int fq, PG8_LAS unsigned char* lds, int wid, int lane) const {
;     ...
; #pragma unroll
;         for (int ai = 0; ai < 2; ++ai)
; #pragma unroll
;             for (int m = 0; m < 4; ++m) {
;                 float q = 0.f;
; #pragma unroll
;                 for (int bj = 0; bj < 2; ++bj)
; #pragma unroll
;                     for (int n = 0; n < 2; ++n) { const f32x4 x = v[ai][bj][m][n]; q += (x[0] * x[0] + x[1] * x[1]) + (x[2] * x[2] + x[3] * x[3]); }
;                 q += swz_xor<16>(q); q = half_sum(q);
;                 if (fq == 0) P[(ai * HALF + wr * 64 + m * 16 + fr) * 4 + wc] = q;
;             }
;     __device__ __forceinline__ void fused(f32x4 (&acc)[2][2][4][2], const Unit& u, int wr, int wc, int fr, int fq, PG8_LAS unsigned char* lds, int wid, int lane) const {
;         const int row0 = u.pm * BM + wr * 64 + fr, col0 = u.pn * BM + wc * 32 + 4 * fq;
; #pragma unroll
;         for (int ai = 0; ai < 2; ++ai)
; #pragma unroll
;             for (int m = 0; m < 4; ++m) {
;                 f32x4 xv[2][2]; const size_t off = (size_t)(row0 + ai * HALF + m * 16) * DM + col0;
; #pragma unroll
;                 for (int bj = 0; bj < 2; ++bj)
; #pragma unroll
;                     for (int n = 0; n < 2; ++n) xv[bj][n] = *(const f32x4*)(xin + off + bj * HALF + n * 16);
; #pragma unroll
;                 for (int bj = 0; bj < 2; ++bj)
; #pragma unroll
;                     for (int n = 0; n < 2; ++n) acc[ai][bj][m][n] += xv[bj][n];
;                 if (m & 1) asm volatile("" ::: "memory");
;             }
.LBB0_152:
	v_readlane_b32 s0, v255, 42
	v_readlane_b32 s36, v252, 3
	s_lshl_b32 s0, s0, 26
	v_readlane_b32 s42, v252, 9
	v_readlane_b32 s43, v252, 10
	s_add_u32 s14, s42, s0
	s_addc_u32 s15, s43, 0
	s_lshl_b32 s28, s26, 8
	s_lshl_b32 s34, s27, 5
	s_add_i32 s0, s28, s13
	v_lshrrev_b32_e32 v130, 2, v251
	v_or_b32_e32 v146, s0, v247
	s_lshl_b32 s35, s2, 8
	v_and_or_b32 v130, v130, 12, s34
	v_or_b32_e32 v130, s35, v130
	v_ashrrev_i32_e32 v147, 31, v146
	v_ashrrev_i32_e32 v131, 31, v130
	v_lshlrev_b64 v[132:133], 12, v[146:147]
	v_lshl_add_u64 v[132:133], s[14:15], 0, v[132:133]
	v_lshlrev_b64 v[148:149], 2, v[130:131]
	v_lshl_add_u64 v[244:245], v[132:133], 0, v[148:149]
	s_waitcnt vmcnt(0)
	s_barrier
	global_load_dwordx4 v[130:133], v[244:245], off
	global_load_dwordx4 v[134:137], v[244:245], off offset:64
	global_load_dwordx4 v[138:141], v[244:245], off offset:512
	global_load_dwordx4 v[142:145], v[244:245], off offset:576
	v_and_b32_e32 v96, 63, v251
	v_readlane_b32 s37, v252, 4
	v_readlane_b32 s38, v252, 5
	v_readlane_b32 s39, v252, 6
	v_readlane_b32 s40, v252, 7
	v_readlane_b32 s41, v252, 8
	v_or_b32_e32 v210, 16, v146
	v_ashrrev_i32_e32 v211, 31, v210
	v_lshlrev_b64 v[210:211], 12, v[210:211]
	v_lshl_add_u64 v[210:211], s[14:15], 0, v[210:211]
	v_lshl_add_u64 v[210:211], v[210:211], 0, v[148:149]
	global_load_dwordx4 v[222:225], v[210:211], off
	global_load_dwordx4 v[218:221], v[210:211], off offset:64
	global_load_dwordx4 v[214:217], v[210:211], off offset:512
	s_nop 0
	global_load_dwordx4 v[210:213], v[210:211], off offset:576
	v_or_b32_e32 v194, 32, v146
	v_ashrrev_i32_e32 v195, 31, v194
	v_lshlrev_b64 v[194:195], 12, v[194:195]
	v_lshl_add_u64 v[194:195], s[14:15], 0, v[194:195]
	v_lshl_add_u64 v[194:195], v[194:195], 0, v[148:149]
	global_load_dwordx4 v[206:209], v[194:195], off
	global_load_dwordx4 v[202:205], v[194:195], off offset:64
	global_load_dwordx4 v[198:201], v[194:195], off offset:512
	s_nop 0
	global_load_dwordx4 v[194:197], v[194:195], off offset:576
	v_or_b32_e32 v178, 48, v146
	v_ashrrev_i32_e32 v179, 31, v178
	v_lshlrev_b64 v[178:179], 12, v[178:179]
	v_lshl_add_u64 v[178:179], s[14:15], 0, v[178:179]
	v_lshl_add_u64 v[178:179], v[178:179], 0, v[148:149]
	global_load_dwordx4 v[190:193], v[178:179], off
	global_load_dwordx4 v[186:189], v[178:179], off offset:64
	global_load_dwordx4 v[182:185], v[178:179], off offset:512
	s_nop 0
	global_load_dwordx4 v[178:181], v[178:179], off offset:576
	s_mov_b64 s[0:1], 0x80000
	v_lshl_add_u64 v[162:163], v[244:245], 0, s[0:1]
	global_load_dwordx4 v[174:177], v[162:163], off
	global_load_dwordx4 v[170:173], v[162:163], off offset:64
	global_load_dwordx4 v[166:169], v[162:163], off offset:512
	s_nop 0
	global_load_dwordx4 v[162:165], v[162:163], off offset:576
	s_mov_b64 s[0:1], 0x90000
	v_lshl_add_u64 v[146:147], v[244:245], 0, s[0:1]
	global_load_dwordx4 v[158:161], v[146:147], off
	global_load_dwordx4 v[154:157], v[146:147], off offset:64
	global_load_dwordx4 v[150:153], v[146:147], off offset:512
	s_nop 0
	global_load_dwordx4 v[146:149], v[146:147], off offset:576
	s_waitcnt vmcnt(20)
	v_pk_add_f32 v[238:239], v[128:129], v[132:133]
	v_pk_add_f32 v[240:241], v[126:127], v[130:131]
	v_pk_add_f32 v[234:235], v[124:125], v[136:137]
	v_pk_add_f32 v[228:229], v[114:115], v[142:143]
	v_pk_add_f32 v[226:227], v[116:117], v[144:145]
	v_pk_add_f32 v[236:237], v[122:123], v[134:135]
	v_pk_add_f32 v[230:231], v[120:121], v[140:141]
	v_pk_add_f32 v[232:233], v[118:119], v[138:139]
	s_mov_b64 s[0:1], 0xa0000
	v_lshl_add_u64 v[130:131], v[244:245], 0, s[0:1]
	s_nop 0
	global_load_dwordx4 v[142:145], v[130:131], off
	global_load_dwordx4 v[138:141], v[130:131], off offset:64
	global_load_dwordx4 v[134:137], v[130:131], off offset:512
	s_nop 0
	global_load_dwordx4 v[130:133], v[130:131], off offset:576
	s_mov_b64 s[0:1], 0xb0000
	v_lshl_add_u64 v[114:115], v[244:245], 0, s[0:1]
	v_mul_f32_e32 v244, v241, v241
	s_nop 0
	global_load_dwordx4 v[126:129], v[114:115], off
	global_load_dwordx4 v[122:125], v[114:115], off offset:64
	global_load_dwordx4 v[118:121], v[114:115], off offset:512
	s_nop 0
	global_load_dwordx4 v[114:117], v[114:115], off offset:576
	v_mul_f32_e32 v245, v239, v239
	v_fmac_f32_e32 v244, v240, v240
	v_fmac_f32_e32 v245, v238, v238
	v_add_f32_e32 v244, v244, v245
	v_mul_f32_e32 v245, v237, v237
	v_mul_f32_e32 v246, v235, v235
	v_fmac_f32_e32 v245, v236, v236
	v_fmac_f32_e32 v246, v234, v234
	v_add_f32_e32 v245, v245, v246
	v_add_f32_e32 v244, v244, v245
	v_mul_f32_e32 v245, v233, v233
	v_mul_f32_e32 v246, v231, v231
	v_fmac_f32_e32 v245, v232, v232
	v_fmac_f32_e32 v246, v230, v230
	v_add_f32_e32 v245, v245, v246
	v_add_f32_e32 v244, v244, v245
	v_mul_f32_e32 v245, v229, v229
	v_mul_f32_e32 v246, v227, v227
	v_fmac_f32_e32 v245, v228, v228
	v_fmac_f32_e32 v246, v226, v226
	v_add_f32_e32 v245, v245, v246
	v_add_f32_e32 v244, v244, v245
	ds_swizzle_b32 v245, v244 offset:swizzle(SWAP,16)
	s_lshl_b32 s0, s27, 2
	v_cmp_gt_u32_e32 vcc, 16, v96
	s_add_i32 s20, s0, 0
	s_waitcnt lgkmcnt(0)
	v_add_f32_e32 v244, v244, v245
	v_mov_b32_e32 v245, v244
	s_nop 1
	v_permlane32_swap_b32_e32 v244, v245
	s_and_saveexec_b64 s[0:1], vcc
	s_lshl_b32 s21, s19, 10
	s_add_i32 s21, s20, s21
	v_lshl_add_u32 v246, v247, 4, s21
	v_add_f32_e32 v244, v244, v245
	ds_write_b32 v246, v244
	s_or_b64 exec, exec, s[0:1]
	s_waitcnt vmcnt(27)
	v_pk_add_f32 v[112:113], v[112:113], v[224:225]
	v_pk_add_f32 v[110:111], v[110:111], v[222:223]
	s_waitcnt vmcnt(24)
; template <int M> __device__ __forceinline__ float swz_xor(float v) { return __int_as_float(__builtin_amdgcn_ds_swizzle(__float_as_int(v), (M << 10) | 0x1f)); }
; __device__ __forceinline__ float half_sum(float v) { auto rr = __builtin_amdgcn_permlane32_swap(__float_as_uint(v), __float_as_uint(v), false, false); return __uint_as_float(rr[0]) + __uint_as_float(rr[1]); }
;     __device__ __forceinline__ bool run(const f32x4 (&v)[2][2][4][2], const Unit& u, int wr, int wc, int fr, int fq, PG8_LAS unsigned char* lds, int wid, int lane) const {
;     ...
; #pragma unroll
;         for (int ai = 0; ai < 2; ++ai)
; #pragma unroll
;             for (int m = 0; m < 4; ++m) {
;                 float q = 0.f;
; #pragma unroll
;                 for (int bj = 0; bj < 2; ++bj)
; #pragma unroll
;                     for (int n = 0; n < 2; ++n) { const f32x4 x = v[ai][bj][m][n]; q += (x[0] * x[0] + x[1] * x[1]) + (x[2] * x[2] + x[3] * x[3]); }
;                 q += swz_xor<16>(q); q = half_sum(q);
;                 if (fq == 0) P[(ai * HALF + wr * 64 + m * 16 + fr) * 4 + wc] = q;
;             }
;     __device__ __forceinline__ void fused(f32x4 (&acc)[2][2][4][2], const Unit& u, int wr, int wc, int fr, int fq, PG8_LAS unsigned char* lds, int wid, int lane) const {
;     ...
;                     for (int n = 0; n < 2; ++n) xv[bj][n] = *(const f32x4*)(xin + off + bj * HALF + n * 16);
; #pragma unroll
;                 for (int bj = 0; bj < 2; ++bj)
; #pragma unroll
;                     for (int n = 0; n < 2; ++n) acc[ai][bj][m][n] += xv[bj][n];
;                 if (m & 1) asm volatile("" ::: "memory");
	v_pk_add_f32 v[98:99], v[98:99], v[210:211]
	v_mul_f32_e32 v210, v111, v111
	v_mul_f32_e32 v211, v113, v113
	v_pk_add_f32 v[108:109], v[108:109], v[220:221]
	v_pk_add_f32 v[106:107], v[106:107], v[218:219]
	v_fmac_f32_e32 v210, v110, v110
	v_fmac_f32_e32 v211, v112, v112
	v_pk_add_f32 v[100:101], v[100:101], v[212:213]
	v_add_f32_e32 v210, v210, v211
	v_mul_f32_e32 v211, v107, v107
	v_mul_f32_e32 v212, v109, v109
	v_fmac_f32_e32 v211, v106, v106
	v_fmac_f32_e32 v212, v108, v108
	v_pk_add_f32 v[104:105], v[104:105], v[216:217]
	v_pk_add_f32 v[102:103], v[102:103], v[214:215]
	v_add_f32_e32 v211, v211, v212
	v_add_f32_e32 v210, v210, v211
	v_mul_f32_e32 v211, v103, v103
	v_mul_f32_e32 v212, v105, v105
	v_fmac_f32_e32 v211, v102, v102
	v_fmac_f32_e32 v212, v104, v104
	v_add_f32_e32 v211, v211, v212
	v_add_f32_e32 v210, v210, v211
	v_mul_f32_e32 v211, v99, v99
	v_mul_f32_e32 v212, v101, v101
	v_fmac_f32_e32 v211, v98, v98
	v_fmac_f32_e32 v212, v100, v100
	v_add_f32_e32 v211, v211, v212
	v_add_f32_e32 v210, v210, v211
	ds_swizzle_b32 v211, v210 offset:swizzle(SWAP,16)
	s_waitcnt lgkmcnt(0)
	v_add_f32_e32 v210, v210, v211
	v_mov_b32_e32 v211, v210
	s_nop 1
	v_permlane32_swap_b32_e32 v210, v211
	s_and_saveexec_b64 s[0:1], vcc
	s_movk_i32 s27, 0x2000
	s_mov_b32 s44, 0x800000
	v_readlane_b32 s45, v255, 35
	s_lshl_b32 s21, s19, 10
	s_add_i32 s21, s20, s21
	v_lshl_add_u32 v212, v247, 4, s21
	v_add_f32_e32 v210, v210, v211
	ds_write_b32 v212, v210 offset:256
	s_or_b64 exec, exec, s[0:1]
	s_waitcnt vmcnt(23)
	v_pk_add_f32 v[94:95], v[94:95], v[208:209]
	v_pk_add_f32 v[92:93], v[92:93], v[206:207]
	s_waitcnt vmcnt(20)
	v_pk_add_f32 v[80:81], v[80:81], v[194:195]
	v_mul_f32_e32 v194, v93, v93
	v_mul_f32_e32 v195, v95, v95
	v_pk_add_f32 v[90:91], v[90:91], v[204:205]
	v_pk_add_f32 v[88:89], v[88:89], v[202:203]
	v_fmac_f32_e32 v194, v92, v92
	v_fmac_f32_e32 v195, v94, v94
	v_pk_add_f32 v[82:83], v[82:83], v[196:197]
	v_add_f32_e32 v194, v194, v195
	v_mul_f32_e32 v195, v89, v89
	v_mul_f32_e32 v196, v91, v91
	v_fmac_f32_e32 v195, v88, v88
	v_fmac_f32_e32 v196, v90, v90
	v_pk_add_f32 v[86:87], v[86:87], v[200:201]
	v_pk_add_f32 v[84:85], v[84:85], v[198:199]
	v_add_f32_e32 v195, v195, v196
	v_add_f32_e32 v194, v194, v195
	v_mul_f32_e32 v195, v85, v85
	v_mul_f32_e32 v196, v87, v87
	v_fmac_f32_e32 v195, v84, v84
	v_fmac_f32_e32 v196, v86, v86
	v_add_f32_e32 v195, v195, v196
	v_add_f32_e32 v194, v194, v195
	v_mul_f32_e32 v195, v81, v81
	v_mul_f32_e32 v196, v83, v83
	v_fmac_f32_e32 v195, v80, v80
	v_fmac_f32_e32 v196, v82, v82
	v_add_f32_e32 v195, v195, v196
	v_add_f32_e32 v194, v194, v195
	ds_swizzle_b32 v195, v194 offset:swizzle(SWAP,16)
	s_waitcnt lgkmcnt(0)
	v_add_f32_e32 v194, v194, v195
	v_mov_b32_e32 v195, v194
	s_nop 1
	v_permlane32_swap_b32_e32 v194, v195
	s_and_saveexec_b64 s[0:1], vcc
	s_lshl_b32 s21, s19, 10
	s_add_i32 s21, s20, s21
	v_lshl_add_u32 v196, v247, 4, s21
	v_add_f32_e32 v194, v194, v195
	ds_write_b32 v196, v194 offset:512
	s_or_b64 exec, exec, s[0:1]
	s_waitcnt vmcnt(19)
	v_pk_add_f32 v[78:79], v[78:79], v[192:193]
	v_pk_add_f32 v[76:77], v[76:77], v[190:191]
	s_waitcnt vmcnt(16)
	v_pk_add_f32 v[64:65], v[64:65], v[178:179]
	v_mul_f32_e32 v178, v77, v77
	v_mul_f32_e32 v179, v79, v79
	v_pk_add_f32 v[74:75], v[74:75], v[188:189]
	v_pk_add_f32 v[72:73], v[72:73], v[186:187]
	v_fmac_f32_e32 v178, v76, v76
	v_fmac_f32_e32 v179, v78, v78
	v_pk_add_f32 v[66:67], v[66:67], v[180:181]
	v_add_f32_e32 v178, v178, v179
	v_mul_f32_e32 v179, v73, v73
	v_mul_f32_e32 v180, v75, v75
	v_fmac_f32_e32 v179, v72, v72
	v_fmac_f32_e32 v180, v74, v74
	v_pk_add_f32 v[70:71], v[70:71], v[184:185]
	v_pk_add_f32 v[68:69], v[68:69], v[182:183]
	v_add_f32_e32 v179, v179, v180
	v_add_f32_e32 v178, v178, v179
	v_mul_f32_e32 v179, v69, v69
	v_mul_f32_e32 v180, v71, v71
	v_fmac_f32_e32 v179, v68, v68
	v_fmac_f32_e32 v180, v70, v70
	v_add_f32_e32 v179, v179, v180
	v_add_f32_e32 v178, v178, v179
	v_mul_f32_e32 v179, v65, v65
	v_mul_f32_e32 v180, v67, v67
	v_fmac_f32_e32 v179, v64, v64
	v_fmac_f32_e32 v180, v66, v66
	v_add_f32_e32 v179, v179, v180
	v_add_f32_e32 v178, v178, v179
	ds_swizzle_b32 v179, v178 offset:swizzle(SWAP,16)
	s_waitcnt lgkmcnt(0)
	v_add_f32_e32 v178, v178, v179
	v_mov_b32_e32 v179, v178
	s_nop 1
	v_permlane32_swap_b32_e32 v178, v179
	s_and_saveexec_b64 s[0:1], vcc
	s_lshl_b32 s21, s19, 10
	s_add_i32 s21, s20, s21
	v_lshl_add_u32 v180, v247, 4, s21
	v_add_f32_e32 v178, v178, v179
	ds_write_b32 v180, v178 offset:768
	s_or_b64 exec, exec, s[0:1]
	s_waitcnt vmcnt(15)
	v_pk_add_f32 v[62:63], v[62:63], v[176:177]
	v_pk_add_f32 v[60:61], v[60:61], v[174:175]
	s_waitcnt vmcnt(12)
	v_pk_add_f32 v[48:49], v[48:49], v[162:163]
	v_mul_f32_e32 v162, v61, v61
	v_mul_f32_e32 v163, v63, v63
	v_pk_add_f32 v[58:59], v[58:59], v[172:173]
	v_pk_add_f32 v[56:57], v[56:57], v[170:171]
	v_fmac_f32_e32 v162, v60, v60
	v_fmac_f32_e32 v163, v62, v62
	v_pk_add_f32 v[50:51], v[50:51], v[164:165]
	v_add_f32_e32 v162, v162, v163
	v_mul_f32_e32 v163, v57, v57
	v_mul_f32_e32 v164, v59, v59
	v_fmac_f32_e32 v163, v56, v56
	v_fmac_f32_e32 v164, v58, v58
	v_pk_add_f32 v[54:55], v[54:55], v[168:169]
	v_pk_add_f32 v[52:53], v[52:53], v[166:167]
	v_add_f32_e32 v163, v163, v164
	v_add_f32_e32 v162, v162, v163
	v_mul_f32_e32 v163, v53, v53
	v_mul_f32_e32 v164, v55, v55
	v_fmac_f32_e32 v163, v52, v52
	v_fmac_f32_e32 v164, v54, v54
	v_add_f32_e32 v163, v163, v164
	v_add_f32_e32 v162, v162, v163
	v_mul_f32_e32 v163, v49, v49
	v_mul_f32_e32 v164, v51, v51
	v_fmac_f32_e32 v163, v48, v48
	v_fmac_f32_e32 v164, v50, v50
	v_add_f32_e32 v163, v163, v164
	v_add_f32_e32 v162, v162, v163
	ds_swizzle_b32 v163, v162 offset:swizzle(SWAP,16)
	s_waitcnt lgkmcnt(0)
; template <int M> __device__ __forceinline__ float swz_xor(float v) { return __int_as_float(__builtin_amdgcn_ds_swizzle(__float_as_int(v), (M << 10) | 0x1f)); }
; __device__ __forceinline__ float half_sum(float v) { auto rr = __builtin_amdgcn_permlane32_swap(__float_as_uint(v), __float_as_uint(v), false, false); return __uint_as_float(rr[0]) + __uint_as_float(rr[1]); }
;     __device__ __forceinline__ bool run(const f32x4 (&v)[2][2][4][2], const Unit& u, int wr, int wc, int fr, int fq, PG8_LAS unsigned char* lds, int wid, int lane) const {
;     ...
; #pragma unroll
;         for (int ai = 0; ai < 2; ++ai)
; #pragma unroll
;             for (int m = 0; m < 4; ++m) {
;                 float q = 0.f;
; #pragma unroll
;                 for (int bj = 0; bj < 2; ++bj)
; #pragma unroll
;                     for (int n = 0; n < 2; ++n) { const f32x4 x = v[ai][bj][m][n]; q += (x[0] * x[0] + x[1] * x[1]) + (x[2] * x[2] + x[3] * x[3]); }
;                 q += swz_xor<16>(q); q = half_sum(q);
;                 if (fq == 0) P[(ai * HALF + wr * 64 + m * 16 + fr) * 4 + wc] = q;
;             }
;         asm volatile("s_waitcnt lgkmcnt(0)" ::: "memory"); __builtin_amdgcn_s_barrier(); asm volatile("" ::: "memory");
;         const int row = wid * 32 + (lane & 31);
;         if (lane < 32) {
;             const float t = (P[row * 4 + 0] + P[row * 4 + 1]) + (P[row * 4 + 2] + P[row * 4 + 3]);
;             __hip_atomic_store(slots + ((size_t)(u.pm * BM + row) * 4 + u.pn), t, __ATOMIC_RELAXED, __HIP_MEMORY_SCOPE_AGENT);
;         }
	v_add_f32_e32 v162, v162, v163
	v_mov_b32_e32 v163, v162
	s_nop 1
	v_permlane32_swap_b32_e32 v162, v163
	s_and_saveexec_b64 s[0:1], vcc
	s_lshl_b32 s21, s19, 10
	s_add_i32 s21, s20, s21
	v_lshl_add_u32 v164, v247, 4, s21
	v_add_f32_e32 v162, v162, v163
	ds_write_b32 v164, v162 offset:2048
	s_or_b64 exec, exec, s[0:1]
	s_waitcnt vmcnt(11)
	v_pk_add_f32 v[46:47], v[46:47], v[160:161]
	v_pk_add_f32 v[44:45], v[44:45], v[158:159]
	s_waitcnt vmcnt(8)
	v_pk_add_f32 v[32:33], v[32:33], v[146:147]
	v_mul_f32_e32 v146, v45, v45
	v_mul_f32_e32 v147, v47, v47
	v_pk_add_f32 v[42:43], v[42:43], v[156:157]
	v_pk_add_f32 v[40:41], v[40:41], v[154:155]
	v_fmac_f32_e32 v146, v44, v44
	v_fmac_f32_e32 v147, v46, v46
	v_pk_add_f32 v[34:35], v[34:35], v[148:149]
	v_add_f32_e32 v146, v146, v147
	v_mul_f32_e32 v147, v41, v41
	v_mul_f32_e32 v148, v43, v43
	v_fmac_f32_e32 v147, v40, v40
	v_fmac_f32_e32 v148, v42, v42
	v_pk_add_f32 v[38:39], v[38:39], v[152:153]
	v_pk_add_f32 v[36:37], v[36:37], v[150:151]
	v_add_f32_e32 v147, v147, v148
	v_add_f32_e32 v146, v146, v147
	v_mul_f32_e32 v147, v37, v37
	v_mul_f32_e32 v148, v39, v39
	v_fmac_f32_e32 v147, v36, v36
	v_fmac_f32_e32 v148, v38, v38
	v_add_f32_e32 v147, v147, v148
	v_add_f32_e32 v146, v146, v147
	v_mul_f32_e32 v147, v33, v33
	v_mul_f32_e32 v148, v35, v35
	v_fmac_f32_e32 v147, v32, v32
	v_fmac_f32_e32 v148, v34, v34
	v_add_f32_e32 v147, v147, v148
	v_add_f32_e32 v146, v146, v147
	ds_swizzle_b32 v147, v146 offset:swizzle(SWAP,16)
	s_waitcnt lgkmcnt(0)
	v_add_f32_e32 v146, v146, v147
	v_mov_b32_e32 v147, v146
	s_nop 1
	v_permlane32_swap_b32_e32 v146, v147
	s_and_saveexec_b64 s[0:1], vcc
	s_lshl_b32 s21, s19, 10
	s_add_i32 s21, s20, s21
	v_lshl_add_u32 v148, v247, 4, s21
	v_add_f32_e32 v146, v146, v147
	ds_write_b32 v148, v146 offset:2304
	s_or_b64 exec, exec, s[0:1]
	s_waitcnt vmcnt(7)
	v_pk_add_f32 v[144:145], v[30:31], v[144:145]
	v_pk_add_f32 v[142:143], v[28:29], v[142:143]
	s_waitcnt vmcnt(6)
	v_pk_add_f32 v[138:139], v[24:25], v[138:139]
	v_mul_f32_e32 v24, v143, v143
	v_mul_f32_e32 v25, v145, v145
	v_pk_add_f32 v[26:27], v[26:27], v[140:141]
	v_fmac_f32_e32 v24, v142, v142
	v_fmac_f32_e32 v25, v144, v144
	v_add_f32_e32 v24, v24, v25
	v_mul_f32_e32 v25, v139, v139
	v_mul_f32_e32 v28, v27, v27
	v_fmac_f32_e32 v25, v138, v138
	v_fmac_f32_e32 v28, v26, v26
	s_waitcnt vmcnt(5)
	v_pk_add_f32 v[22:23], v[22:23], v[136:137]
	v_pk_add_f32 v[20:21], v[20:21], v[134:135]
	v_add_f32_e32 v25, v25, v28
	v_add_f32_e32 v24, v24, v25
	v_mul_f32_e32 v25, v21, v21
	v_mul_f32_e32 v28, v23, v23
	v_fmac_f32_e32 v25, v20, v20
	v_fmac_f32_e32 v28, v22, v22
	s_waitcnt vmcnt(4)
	v_pk_add_f32 v[18:19], v[18:19], v[132:133]
	v_pk_add_f32 v[16:17], v[16:17], v[130:131]
	v_add_f32_e32 v25, v25, v28
	v_add_f32_e32 v24, v24, v25
	v_mul_f32_e32 v25, v17, v17
	v_mul_f32_e32 v28, v19, v19
	v_fmac_f32_e32 v25, v16, v16
	v_fmac_f32_e32 v28, v18, v18
	v_add_f32_e32 v25, v25, v28
	v_add_f32_e32 v24, v24, v25
	ds_swizzle_b32 v25, v24 offset:swizzle(SWAP,16)
	s_waitcnt lgkmcnt(0)
	v_add_f32_e32 v24, v24, v25
	v_mov_b32_e32 v25, v24
	s_nop 1
	v_permlane32_swap_b32_e32 v24, v25
	s_and_saveexec_b64 s[0:1], vcc
	s_lshl_b32 s21, s19, 10
	s_add_i32 s21, s20, s21
	v_lshl_add_u32 v28, v247, 4, s21
	v_add_f32_e32 v24, v24, v25
	ds_write_b32 v28, v24 offset:2560
	s_or_b64 exec, exec, s[0:1]
	s_waitcnt vmcnt(3)
	v_pk_add_f32 v[128:129], v[14:15], v[128:129]
	v_pk_add_f32 v[126:127], v[12:13], v[126:127]
	s_waitcnt vmcnt(0)
	v_pk_add_f32 v[28:29], v[0:1], v[114:115]
	v_mul_f32_e32 v0, v127, v127
	v_mul_f32_e32 v1, v129, v129
	v_pk_add_f32 v[124:125], v[10:11], v[124:125]
	v_pk_add_f32 v[122:123], v[8:9], v[122:123]
	v_fmac_f32_e32 v0, v126, v126
	v_fmac_f32_e32 v1, v128, v128
	v_pk_add_f32 v[24:25], v[2:3], v[116:117]
	v_add_f32_e32 v0, v0, v1
	v_mul_f32_e32 v1, v123, v123
	v_mul_f32_e32 v2, v125, v125
	v_fmac_f32_e32 v1, v122, v122
	v_fmac_f32_e32 v2, v124, v124
	v_pk_add_f32 v[30:31], v[6:7], v[120:121]
	v_pk_add_f32 v[118:119], v[4:5], v[118:119]
	v_add_f32_e32 v1, v1, v2
	v_add_f32_e32 v0, v0, v1
	v_mul_f32_e32 v1, v119, v119
	v_mul_f32_e32 v2, v31, v31
	v_fmac_f32_e32 v1, v118, v118
	v_fmac_f32_e32 v2, v30, v30
	v_add_f32_e32 v1, v1, v2
	v_add_f32_e32 v0, v0, v1
	v_mul_f32_e32 v1, v29, v29
	v_mul_f32_e32 v2, v25, v25
	v_fmac_f32_e32 v1, v28, v28
	v_fmac_f32_e32 v2, v24, v24
	v_add_f32_e32 v1, v1, v2
	v_add_f32_e32 v0, v0, v1
	ds_swizzle_b32 v1, v0 offset:swizzle(SWAP,16)
	s_waitcnt lgkmcnt(0)
	v_add_f32_e32 v0, v0, v1
	v_mov_b32_e32 v1, v0
	s_nop 1
	v_permlane32_swap_b32_e32 v0, v1
	s_and_saveexec_b64 s[0:1], vcc
	s_lshl_b32 s19, s19, 10
	s_add_i32 s20, s20, s19
	v_lshl_add_u32 v2, v247, 4, s20
	v_add_f32_e32 v0, v0, v1
	ds_write_b32 v2, v0 offset:2816
	s_or_b64 exec, exec, s[0:1]
	v_and_b32_e32 v0, 31, v251
	s_waitcnt lgkmcnt(0)
	s_barrier
	v_lshl_or_b32 v2, s3, 5, v0
	v_add_u32_e32 v0, s28, v2
	v_cmp_gt_u32_e64 s[0:1], 32, v96
	v_ashrrev_i32_e32 v1, 31, v0
	s_and_saveexec_b64 s[20:21], s[0:1]
	s_cbranch_execz .LBB0_170
	v_lshl_add_u32 v3, v2, 4, 0
	ds_read_b128 v[4:7], v3
	v_readlane_b32 s36, v253, 29
	v_readlane_b32 s37, v253, 30
	s_ashr_i32 s3, s2, 31
	s_waitcnt lgkmcnt(0)
	v_mov_b32_e32 v8, v5
	v_mov_b32_e32 v9, v6
	v_mov_b32_e32 v5, v7
	v_pk_add_f32 v[4:5], v[8:9], v[4:5]
	v_lshl_add_u64 v[6:7], v[0:1], 4, s[36:37]
	v_pk_add_f32 v[4:5], v[4:5], v[4:5] op_sel:[0,1] op_sel_hi:[1,0]
	v_lshl_add_u64 v[6:7], s[2:3], 2, v[6:7]
	global_store_dword v[6:7], v4, off sc1

; template <int M> __device__ __forceinline__ float swz_xor(float v) { return __int_as_float(__builtin_amdgcn_ds_swizzle(__float_as_int(v), (M << 10) | 0x1f)); }
; __device__ __forceinline__ float half_sum(float v) { auto rr = __builtin_amdgcn_permlane32_swap(__float_as_uint(v), __float_as_uint(v), false, false); return __uint_as_float(rr[0]) + __uint_as_float(rr[1]); }
;     __device__ __forceinline__ bool run(const f32x4 (&v)[2][2][4][2], const Unit& u, int wr, int wc, int fr, int fq, PG8_LAS unsigned char* lds, int wid, int lane) const {
;     ...
; #pragma unroll
;         for (int ai = 0; ai < 2; ++ai)
; #pragma unroll
;             for (int m = 0; m < 4; ++m) {
;                 float q = 0.f;
; #pragma unroll
;                 for (int bj = 0; bj < 2; ++bj)
; #pragma unroll
;                     for (int n = 0; n < 2; ++n) { const f32x4 x = v[ai][bj][m][n]; q += (x[0] * x[0] + x[1] * x[1]) + (x[2] * x[2] + x[3] * x[3]); }
;                 q += swz_xor<16>(q); q = half_sum(q);
;                 if (fq == 0) P[(ai * HALF + wr * 64 + m * 16 + fr) * 4 + wc] = q;
;             }
;     __device__ __forceinline__ void fused(f32x4 (&acc)[2][2][4][2], const Unit& u, int wr, int wc, int fr, int fq, PG8_LAS unsigned char* lds, int wid, int lane) const {
;         const int row0 = u.pm * BM + wr * 64 + fr, col0 = u.pn * BM + wc * 32 + 4 * fq;
; #pragma unroll
;         for (int ai = 0; ai < 2; ++ai)
; #pragma unroll
;             for (int m = 0; m < 4; ++m) {
;                 f32x4 xv[2][2]; const size_t off = (size_t)(row0 + ai * HALF + m * 16) * DM + col0;
; #pragma unroll
;                 for (int bj = 0; bj < 2; ++bj)
; #pragma unroll
;                     for (int n = 0; n < 2; ++n) xv[bj][n] = *(const f32x4*)(xin + off + bj * HALF + n * 16);
; #pragma unroll
;                 for (int bj = 0; bj < 2; ++bj)
; #pragma unroll
;                     for (int n = 0; n < 2; ++n) acc[ai][bj][m][n] += xv[bj][n];
;                 if (m & 1) asm volatile("" ::: "memory");
;             }
.LBB0_231:
	v_readlane_b32 s0, v255, 31
	s_lshl_b32 s28, s0, 24
	s_lshl_b64 s[14:15], s[28:29], 2
	v_readlane_b32 s52, v253, 36
	v_readlane_b32 s53, v253, 37
	s_add_u32 s0, s52, s14
	s_addc_u32 s1, s53, s15
	s_lshl_b32 s10, s26, 8
	s_lshl_b32 s11, s27, 5
	s_add_i32 s12, s10, s13
	v_lshrrev_b32_e32 v130, 2, v251
	v_or_b32_e32 v146, s12, v216
	s_lshl_b32 s12, s2, 8
	v_and_or_b32 v130, v130, 12, s11
	v_or_b32_e32 v130, s12, v130
	v_ashrrev_i32_e32 v147, 31, v146
	v_ashrrev_i32_e32 v131, 31, v130
	v_lshlrev_b64 v[132:133], 12, v[146:147]
	v_lshl_add_u64 v[132:133], s[0:1], 0, v[132:133]
	v_lshlrev_b64 v[148:149], 2, v[130:131]
	v_lshl_add_u64 v[244:245], v[132:133], 0, v[148:149]
	s_waitcnt vmcnt(0)
	s_barrier
	global_load_dwordx4 v[130:133], v[244:245], off
	global_load_dwordx4 v[134:137], v[244:245], off offset:64
	global_load_dwordx4 v[138:141], v[244:245], off offset:512
	global_load_dwordx4 v[142:145], v[244:245], off offset:576
	v_mov_b32_e32 v247, v216
	v_and_b32_e32 v96, 63, v251
	v_readlane_b32 s54, v253, 38
	v_readlane_b32 s55, v253, 39
	v_readlane_b32 s56, v253, 40
	v_readlane_b32 s57, v253, 41
	v_readlane_b32 s58, v253, 42
	v_readlane_b32 s59, v253, 43
	v_readlane_b32 s60, v253, 44
	v_readlane_b32 s61, v253, 45
	v_readlane_b32 s62, v253, 46
	v_readlane_b32 s63, v253, 47
	v_readlane_b32 s64, v253, 48
	v_readlane_b32 s65, v253, 49
	v_readlane_b32 s66, v253, 50
	v_readlane_b32 s67, v253, 51
	v_or_b32_e32 v226, 16, v146
	v_ashrrev_i32_e32 v227, 31, v226
	v_lshlrev_b64 v[226:227], 12, v[226:227]
	v_lshl_add_u64 v[226:227], s[0:1], 0, v[226:227]
	v_lshl_add_u64 v[226:227], v[226:227], 0, v[148:149]
	global_load_dwordx4 v[238:241], v[226:227], off
	global_load_dwordx4 v[234:237], v[226:227], off offset:64
	global_load_dwordx4 v[230:233], v[226:227], off offset:512
	s_nop 0
	global_load_dwordx4 v[226:229], v[226:227], off offset:576
	v_or_b32_e32 v210, 32, v146
	v_ashrrev_i32_e32 v211, 31, v210
	v_lshlrev_b64 v[210:211], 12, v[210:211]
	v_lshl_add_u64 v[210:211], s[0:1], 0, v[210:211]
	v_lshl_add_u64 v[210:211], v[210:211], 0, v[148:149]
	global_load_dwordx4 v[222:225], v[210:211], off
	global_load_dwordx4 v[218:221], v[210:211], off offset:64
	global_load_dwordx4 v[214:217], v[210:211], off offset:512
	s_nop 0
	global_load_dwordx4 v[210:213], v[210:211], off offset:576
	v_or_b32_e32 v194, 48, v146
	v_ashrrev_i32_e32 v195, 31, v194
	v_lshlrev_b64 v[194:195], 12, v[194:195]
	v_lshl_add_u64 v[194:195], s[0:1], 0, v[194:195]
	v_lshl_add_u64 v[194:195], v[194:195], 0, v[148:149]
	global_load_dwordx4 v[206:209], v[194:195], off
	global_load_dwordx4 v[202:205], v[194:195], off offset:64
	global_load_dwordx4 v[198:201], v[194:195], off offset:512
	s_nop 0
	global_load_dwordx4 v[194:197], v[194:195], off offset:576
	s_mov_b64 s[0:1], 0x80000
	v_lshl_add_u64 v[178:179], v[244:245], 0, s[0:1]
	global_load_dwordx4 v[190:193], v[178:179], off
	global_load_dwordx4 v[186:189], v[178:179], off offset:64
	global_load_dwordx4 v[182:185], v[178:179], off offset:512
	s_nop 0
	global_load_dwordx4 v[178:181], v[178:179], off offset:576
	s_mov_b64 s[0:1], 0x90000
	v_lshl_add_u64 v[162:163], v[244:245], 0, s[0:1]
	global_load_dwordx4 v[174:177], v[162:163], off
	global_load_dwordx4 v[170:173], v[162:163], off offset:64
	global_load_dwordx4 v[166:169], v[162:163], off offset:512
	s_nop 0
	global_load_dwordx4 v[162:165], v[162:163], off offset:576
	s_mov_b64 s[0:1], 0xa0000
	v_lshl_add_u64 v[146:147], v[244:245], 0, s[0:1]
	global_load_dwordx4 v[158:161], v[146:147], off
	global_load_dwordx4 v[154:157], v[146:147], off offset:64
	global_load_dwordx4 v[150:153], v[146:147], off offset:512
	s_nop 0
	global_load_dwordx4 v[146:149], v[146:147], off offset:576
	s_waitcnt vmcnt(24)
	v_pk_add_f32 v[126:127], v[126:127], v[130:131]
	v_pk_add_f32 v[128:129], v[128:129], v[132:133]
	v_pk_add_f32 v[124:125], v[124:125], v[136:137]
	v_pk_add_f32 v[122:123], v[122:123], v[134:135]
	v_pk_add_f32 v[120:121], v[120:121], v[140:141]
	v_pk_add_f32 v[118:119], v[118:119], v[138:139]
	v_pk_add_f32 v[116:117], v[116:117], v[144:145]
	v_pk_add_f32 v[114:115], v[114:115], v[142:143]
	s_mov_b64 s[0:1], 0xb0000
	v_lshl_add_u64 v[130:131], v[244:245], 0, s[0:1]
	s_nop 0
	global_load_dwordx4 v[142:145], v[130:131], off
	global_load_dwordx4 v[138:141], v[130:131], off offset:64
	global_load_dwordx4 v[134:137], v[130:131], off offset:512
	s_nop 0
	global_load_dwordx4 v[130:133], v[130:131], off offset:576
	v_mul_f32_e32 v244, v127, v127
	v_mul_f32_e32 v245, v129, v129
	v_fmac_f32_e32 v244, v126, v126
	v_fmac_f32_e32 v245, v128, v128
	v_add_f32_e32 v244, v244, v245
	v_mul_f32_e32 v245, v123, v123
	v_mul_f32_e32 v246, v125, v125
	v_fmac_f32_e32 v245, v122, v122
	v_fmac_f32_e32 v246, v124, v124
	v_add_f32_e32 v245, v245, v246
	v_add_f32_e32 v244, v244, v245
	v_mul_f32_e32 v245, v119, v119
	v_mul_f32_e32 v246, v121, v121
	v_fmac_f32_e32 v245, v118, v118
	v_fmac_f32_e32 v246, v120, v120
	v_add_f32_e32 v245, v245, v246
	v_add_f32_e32 v244, v244, v245
	v_mul_f32_e32 v245, v115, v115
	v_mul_f32_e32 v246, v117, v117
	v_fmac_f32_e32 v245, v114, v114
	v_fmac_f32_e32 v246, v116, v116
	v_add_f32_e32 v245, v245, v246
	v_add_f32_e32 v244, v244, v245
	ds_swizzle_b32 v245, v244 offset:swizzle(SWAP,16)
	s_lshl_b32 s0, s27, 2
	v_cmp_gt_u32_e32 vcc, 16, v96
	s_add_i32 s20, s0, 0
	s_waitcnt lgkmcnt(0)
	v_add_f32_e32 v244, v244, v245
	v_mov_b32_e32 v245, v244
	s_nop 1
	v_permlane32_swap_b32_e32 v244, v245
	s_and_saveexec_b64 s[0:1], vcc
	s_lshl_b32 s21, s19, 10
	s_add_i32 s21, s20, s21
	v_lshl_add_u32 v246, v247, 4, s21
	v_add_f32_e32 v244, v244, v245
	ds_write_b32 v246, v244
	s_or_b64 exec, exec, s[0:1]
	s_waitcnt vmcnt(27)
; template <int M> __device__ __forceinline__ float swz_xor(float v) { return __int_as_float(__builtin_amdgcn_ds_swizzle(__float_as_int(v), (M << 10) | 0x1f)); }
; __device__ __forceinline__ float half_sum(float v) { auto rr = __builtin_amdgcn_permlane32_swap(__float_as_uint(v), __float_as_uint(v), false, false); return __uint_as_float(rr[0]) + __uint_as_float(rr[1]); }
;     __device__ __forceinline__ bool run(const f32x4 (&v)[2][2][4][2], const Unit& u, int wr, int wc, int fr, int fq, PG8_LAS unsigned char* lds, int wid, int lane) const {
;     ...
; #pragma unroll
;         for (int ai = 0; ai < 2; ++ai)
; #pragma unroll
;             for (int m = 0; m < 4; ++m) {
;                 float q = 0.f;
; #pragma unroll
;                 for (int bj = 0; bj < 2; ++bj)
; #pragma unroll
;                     for (int n = 0; n < 2; ++n) { const f32x4 x = v[ai][bj][m][n]; q += (x[0] * x[0] + x[1] * x[1]) + (x[2] * x[2] + x[3] * x[3]); }
;                 q += swz_xor<16>(q); q = half_sum(q);
;                 if (fq == 0) P[(ai * HALF + wr * 64 + m * 16 + fr) * 4 + wc] = q;
;             }
	v_pk_add_f32 v[112:113], v[112:113], v[240:241]
	v_pk_add_f32 v[110:111], v[110:111], v[238:239]
	s_waitcnt vmcnt(24)
	v_pk_add_f32 v[98:99], v[98:99], v[226:227]
	v_mul_f32_e32 v226, v111, v111
	v_mul_f32_e32 v227, v113, v113
	v_pk_add_f32 v[108:109], v[108:109], v[236:237]
	v_pk_add_f32 v[106:107], v[106:107], v[234:235]
	v_fmac_f32_e32 v226, v110, v110
	v_fmac_f32_e32 v227, v112, v112
	v_pk_add_f32 v[100:101], v[100:101], v[228:229]
	v_add_f32_e32 v226, v226, v227
	v_mul_f32_e32 v227, v107, v107
	v_mul_f32_e32 v228, v109, v109
	v_fmac_f32_e32 v227, v106, v106
	v_fmac_f32_e32 v228, v108, v108
	v_pk_add_f32 v[104:105], v[104:105], v[232:233]
	v_pk_add_f32 v[102:103], v[102:103], v[230:231]
	v_add_f32_e32 v227, v227, v228
	v_add_f32_e32 v226, v226, v227
	v_mul_f32_e32 v227, v103, v103
	v_mul_f32_e32 v228, v105, v105
	v_fmac_f32_e32 v227, v102, v102
	v_fmac_f32_e32 v228, v104, v104
	v_add_f32_e32 v227, v227, v228
	v_add_f32_e32 v226, v226, v227
	v_mul_f32_e32 v227, v99, v99
	v_mul_f32_e32 v228, v101, v101
	v_fmac_f32_e32 v227, v98, v98
	v_fmac_f32_e32 v228, v100, v100
	v_add_f32_e32 v227, v227, v228
	v_add_f32_e32 v226, v226, v227
	ds_swizzle_b32 v227, v226 offset:swizzle(SWAP,16)
	s_waitcnt lgkmcnt(0)
	v_add_f32_e32 v226, v226, v227
	v_mov_b32_e32 v227, v226
	s_nop 1
	v_permlane32_swap_b32_e32 v226, v227
	s_and_saveexec_b64 s[0:1], vcc
	s_movk_i32 s27, 0x2000
	s_mov_b32 s44, 0x800000
	v_readlane_b32 s45, v255, 35
	s_lshl_b32 s21, s19, 10
	s_add_i32 s21, s20, s21
	v_lshl_add_u32 v228, v247, 4, s21
	v_add_f32_e32 v226, v226, v227
	ds_write_b32 v228, v226 offset:256
	s_or_b64 exec, exec, s[0:1]
	s_waitcnt vmcnt(23)
	v_pk_add_f32 v[94:95], v[94:95], v[224:225]
	v_pk_add_f32 v[92:93], v[92:93], v[222:223]
	s_waitcnt vmcnt(20)
	v_pk_add_f32 v[80:81], v[80:81], v[210:211]
	v_mul_f32_e32 v210, v93, v93
	v_mul_f32_e32 v211, v95, v95
	v_pk_add_f32 v[90:91], v[90:91], v[220:221]
	v_pk_add_f32 v[88:89], v[88:89], v[218:219]
	v_fmac_f32_e32 v210, v92, v92
	v_fmac_f32_e32 v211, v94, v94
	v_pk_add_f32 v[82:83], v[82:83], v[212:213]
	v_add_f32_e32 v210, v210, v211
	v_mul_f32_e32 v211, v89, v89
	v_mul_f32_e32 v212, v91, v91
	v_fmac_f32_e32 v211, v88, v88
	v_fmac_f32_e32 v212, v90, v90
	v_pk_add_f32 v[86:87], v[86:87], v[216:217]
	v_pk_add_f32 v[84:85], v[84:85], v[214:215]
	v_add_f32_e32 v211, v211, v212
	v_add_f32_e32 v210, v210, v211
	v_mul_f32_e32 v211, v85, v85
	v_mul_f32_e32 v212, v87, v87
	v_fmac_f32_e32 v211, v84, v84
	v_fmac_f32_e32 v212, v86, v86
	v_add_f32_e32 v211, v211, v212
	v_add_f32_e32 v210, v210, v211
	v_mul_f32_e32 v211, v81, v81
	v_mul_f32_e32 v212, v83, v83
	v_fmac_f32_e32 v211, v80, v80
	v_fmac_f32_e32 v212, v82, v82
	v_add_f32_e32 v211, v211, v212
	v_add_f32_e32 v210, v210, v211
	ds_swizzle_b32 v211, v210 offset:swizzle(SWAP,16)
	s_waitcnt lgkmcnt(0)
	v_add_f32_e32 v210, v210, v211
	v_mov_b32_e32 v211, v210
	s_nop 1
	v_permlane32_swap_b32_e32 v210, v211
	s_and_saveexec_b64 s[0:1], vcc
	s_mov_b64 s[62:63], 0x80
	s_lshl_b32 s21, s19, 10
	s_add_i32 s21, s20, s21
	v_lshl_add_u32 v212, v247, 4, s21
	v_add_f32_e32 v210, v210, v211
	ds_write_b32 v212, v210 offset:512
	s_or_b64 exec, exec, s[0:1]
	s_waitcnt vmcnt(19)
	v_pk_add_f32 v[78:79], v[78:79], v[208:209]
	v_pk_add_f32 v[76:77], v[76:77], v[206:207]
	s_waitcnt vmcnt(16)
	v_pk_add_f32 v[64:65], v[64:65], v[194:195]
	v_mul_f32_e32 v194, v77, v77
	v_mul_f32_e32 v195, v79, v79
	v_pk_add_f32 v[74:75], v[74:75], v[204:205]
	v_pk_add_f32 v[72:73], v[72:73], v[202:203]
	v_fmac_f32_e32 v194, v76, v76
	v_fmac_f32_e32 v195, v78, v78
	v_pk_add_f32 v[66:67], v[66:67], v[196:197]
	v_add_f32_e32 v194, v194, v195
	v_mul_f32_e32 v195, v73, v73
	v_mul_f32_e32 v196, v75, v75
	v_fmac_f32_e32 v195, v72, v72
	v_fmac_f32_e32 v196, v74, v74
	v_pk_add_f32 v[70:71], v[70:71], v[200:201]
	v_pk_add_f32 v[68:69], v[68:69], v[198:199]
	v_add_f32_e32 v195, v195, v196
	v_add_f32_e32 v194, v194, v195
	v_mul_f32_e32 v195, v69, v69
	v_mul_f32_e32 v196, v71, v71
	v_fmac_f32_e32 v195, v68, v68
	v_fmac_f32_e32 v196, v70, v70
	v_add_f32_e32 v195, v195, v196
	v_add_f32_e32 v194, v194, v195
	v_mul_f32_e32 v195, v65, v65
	v_mul_f32_e32 v196, v67, v67
	v_fmac_f32_e32 v195, v64, v64
	v_fmac_f32_e32 v196, v66, v66
	v_add_f32_e32 v195, v195, v196
	v_add_f32_e32 v194, v194, v195
	ds_swizzle_b32 v195, v194 offset:swizzle(SWAP,16)
	s_waitcnt lgkmcnt(0)
	v_add_f32_e32 v194, v194, v195
	v_mov_b32_e32 v195, v194
	s_nop 1
	v_permlane32_swap_b32_e32 v194, v195
	s_and_saveexec_b64 s[0:1], vcc
	s_lshl_b32 s21, s19, 10
	s_add_i32 s21, s20, s21
	v_lshl_add_u32 v196, v247, 4, s21
	v_add_f32_e32 v194, v194, v195
	ds_write_b32 v196, v194 offset:768
	s_or_b64 exec, exec, s[0:1]
	s_waitcnt vmcnt(15)
	v_pk_add_f32 v[62:63], v[62:63], v[192:193]
	v_pk_add_f32 v[60:61], v[60:61], v[190:191]
	s_waitcnt vmcnt(12)
	v_pk_add_f32 v[48:49], v[48:49], v[178:179]
	v_mul_f32_e32 v178, v61, v61
	v_mul_f32_e32 v179, v63, v63
	v_pk_add_f32 v[58:59], v[58:59], v[188:189]
	v_pk_add_f32 v[56:57], v[56:57], v[186:187]
	v_fmac_f32_e32 v178, v60, v60
	v_fmac_f32_e32 v179, v62, v62
	v_pk_add_f32 v[50:51], v[50:51], v[180:181]
	v_add_f32_e32 v178, v178, v179
	v_mul_f32_e32 v179, v57, v57
	v_mul_f32_e32 v180, v59, v59
	v_fmac_f32_e32 v179, v56, v56
	v_fmac_f32_e32 v180, v58, v58
	v_pk_add_f32 v[54:55], v[54:55], v[184:185]
	v_pk_add_f32 v[52:53], v[52:53], v[182:183]
	v_add_f32_e32 v179, v179, v180
	v_add_f32_e32 v178, v178, v179
	v_mul_f32_e32 v179, v53, v53
	v_mul_f32_e32 v180, v55, v55
	v_fmac_f32_e32 v179, v52, v52
	v_fmac_f32_e32 v180, v54, v54
	v_add_f32_e32 v179, v179, v180
	v_add_f32_e32 v178, v178, v179
	v_mul_f32_e32 v179, v49, v49
	v_mul_f32_e32 v180, v51, v51
	v_fmac_f32_e32 v179, v48, v48
	v_fmac_f32_e32 v180, v50, v50
	v_add_f32_e32 v179, v179, v180
	v_add_f32_e32 v178, v178, v179
	ds_swizzle_b32 v179, v178 offset:swizzle(SWAP,16)
	s_waitcnt lgkmcnt(0)
; template <int M> __device__ __forceinline__ float swz_xor(float v) { return __int_as_float(__builtin_amdgcn_ds_swizzle(__float_as_int(v), (M << 10) | 0x1f)); }
; __device__ __forceinline__ float half_sum(float v) { auto rr = __builtin_amdgcn_permlane32_swap(__float_as_uint(v), __float_as_uint(v), false, false); return __uint_as_float(rr[0]) + __uint_as_float(rr[1]); }
;     __device__ __forceinline__ bool run(const f32x4 (&v)[2][2][4][2], const Unit& u, int wr, int wc, int fr, int fq, PG8_LAS unsigned char* lds, int wid, int lane) const {
;     ...
; #pragma unroll
;         for (int ai = 0; ai < 2; ++ai)
; #pragma unroll
;             for (int m = 0; m < 4; ++m) {
;                 float q = 0.f;
; #pragma unroll
;                 for (int bj = 0; bj < 2; ++bj)
; #pragma unroll
;                     for (int n = 0; n < 2; ++n) { const f32x4 x = v[ai][bj][m][n]; q += (x[0] * x[0] + x[1] * x[1]) + (x[2] * x[2] + x[3] * x[3]); }
;                 q += swz_xor<16>(q); q = half_sum(q);
;                 if (fq == 0) P[(ai * HALF + wr * 64 + m * 16 + fr) * 4 + wc] = q;
;             }
;         asm volatile("s_waitcnt lgkmcnt(0)" ::: "memory"); __builtin_amdgcn_s_barrier(); asm volatile("" ::: "memory");
;         const int row = wid * 32 + (lane & 31);
;         if (lane < 32) {
;             const float t = (P[row * 4 + 0] + P[row * 4 + 1]) + (P[row * 4 + 2] + P[row * 4 + 3]);
;             __hip_atomic_store(slots + ((size_t)(u.pm * BM + row) * 4 + u.pn), t, __ATOMIC_RELAXED, __HIP_MEMORY_SCOPE_AGENT);
;         }
	v_add_f32_e32 v178, v178, v179
	v_mov_b32_e32 v179, v178
	s_nop 1
	v_permlane32_swap_b32_e32 v178, v179
	s_and_saveexec_b64 s[0:1], vcc
	s_lshl_b32 s21, s19, 10
	s_add_i32 s21, s20, s21
	v_lshl_add_u32 v180, v247, 4, s21
	v_add_f32_e32 v178, v178, v179
	ds_write_b32 v180, v178 offset:2048
	s_or_b64 exec, exec, s[0:1]
	s_waitcnt vmcnt(11)
	v_pk_add_f32 v[46:47], v[46:47], v[176:177]
	v_pk_add_f32 v[44:45], v[44:45], v[174:175]
	s_waitcnt vmcnt(8)
	v_pk_add_f32 v[32:33], v[32:33], v[162:163]
	v_mul_f32_e32 v162, v45, v45
	v_mul_f32_e32 v163, v47, v47
	v_pk_add_f32 v[42:43], v[42:43], v[172:173]
	v_pk_add_f32 v[40:41], v[40:41], v[170:171]
	v_fmac_f32_e32 v162, v44, v44
	v_fmac_f32_e32 v163, v46, v46
	v_pk_add_f32 v[34:35], v[34:35], v[164:165]
	v_add_f32_e32 v162, v162, v163
	v_mul_f32_e32 v163, v41, v41
	v_mul_f32_e32 v164, v43, v43
	v_fmac_f32_e32 v163, v40, v40
	v_fmac_f32_e32 v164, v42, v42
	v_pk_add_f32 v[38:39], v[38:39], v[168:169]
	v_pk_add_f32 v[36:37], v[36:37], v[166:167]
	v_add_f32_e32 v163, v163, v164
	v_add_f32_e32 v162, v162, v163
	v_mul_f32_e32 v163, v37, v37
	v_mul_f32_e32 v164, v39, v39
	v_fmac_f32_e32 v163, v36, v36
	v_fmac_f32_e32 v164, v38, v38
	v_add_f32_e32 v163, v163, v164
	v_add_f32_e32 v162, v162, v163
	v_mul_f32_e32 v163, v33, v33
	v_mul_f32_e32 v164, v35, v35
	v_fmac_f32_e32 v163, v32, v32
	v_fmac_f32_e32 v164, v34, v34
	v_add_f32_e32 v163, v163, v164
	v_add_f32_e32 v162, v162, v163
	ds_swizzle_b32 v163, v162 offset:swizzle(SWAP,16)
	s_waitcnt lgkmcnt(0)
	v_add_f32_e32 v162, v162, v163
	v_mov_b32_e32 v163, v162
	s_nop 1
	v_permlane32_swap_b32_e32 v162, v163
	s_and_saveexec_b64 s[0:1], vcc
	s_lshl_b32 s21, s19, 10
	s_add_i32 s21, s20, s21
	v_lshl_add_u32 v164, v247, 4, s21
	v_add_f32_e32 v162, v162, v163
	ds_write_b32 v164, v162 offset:2304
	s_or_b64 exec, exec, s[0:1]
	s_waitcnt vmcnt(7)
	v_pk_add_f32 v[30:31], v[30:31], v[160:161]
	v_pk_add_f32 v[28:29], v[28:29], v[158:159]
	s_waitcnt vmcnt(4)
	v_pk_add_f32 v[16:17], v[16:17], v[146:147]
	v_mul_f32_e32 v146, v29, v29
	v_mul_f32_e32 v147, v31, v31
	v_pk_add_f32 v[26:27], v[26:27], v[156:157]
	v_pk_add_f32 v[24:25], v[24:25], v[154:155]
	v_fmac_f32_e32 v146, v28, v28
	v_fmac_f32_e32 v147, v30, v30
	v_pk_add_f32 v[18:19], v[18:19], v[148:149]
	v_add_f32_e32 v146, v146, v147
	v_mul_f32_e32 v147, v25, v25
	v_mul_f32_e32 v148, v27, v27
	v_fmac_f32_e32 v147, v24, v24
	v_fmac_f32_e32 v148, v26, v26
	v_pk_add_f32 v[22:23], v[22:23], v[152:153]
	v_pk_add_f32 v[20:21], v[20:21], v[150:151]
	v_add_f32_e32 v147, v147, v148
	v_add_f32_e32 v146, v146, v147
	v_mul_f32_e32 v147, v21, v21
	v_mul_f32_e32 v148, v23, v23
	v_fmac_f32_e32 v147, v20, v20
	v_fmac_f32_e32 v148, v22, v22
	v_add_f32_e32 v147, v147, v148
	v_add_f32_e32 v146, v146, v147
	v_mul_f32_e32 v147, v17, v17
	v_mul_f32_e32 v148, v19, v19
	v_fmac_f32_e32 v147, v16, v16
	v_fmac_f32_e32 v148, v18, v18
	v_add_f32_e32 v147, v147, v148
	v_add_f32_e32 v146, v146, v147
	ds_swizzle_b32 v147, v146 offset:swizzle(SWAP,16)
	s_waitcnt lgkmcnt(0)
	v_add_f32_e32 v146, v146, v147
	v_mov_b32_e32 v147, v146
	s_nop 1
	v_permlane32_swap_b32_e32 v146, v147
	s_and_saveexec_b64 s[0:1], vcc
	s_lshl_b32 s21, s19, 10
	s_add_i32 s21, s20, s21
	v_lshl_add_u32 v148, v247, 4, s21
	v_add_f32_e32 v146, v146, v147
	ds_write_b32 v148, v146 offset:2560
	s_or_b64 exec, exec, s[0:1]
	s_waitcnt vmcnt(3)
	v_pk_add_f32 v[14:15], v[14:15], v[144:145]
	v_pk_add_f32 v[12:13], v[12:13], v[142:143]
	s_waitcnt vmcnt(0)
	v_pk_add_f32 v[0:1], v[0:1], v[130:131]
	v_mul_f32_e32 v130, v13, v13
	v_mul_f32_e32 v131, v15, v15
	v_pk_add_f32 v[10:11], v[10:11], v[140:141]
	v_pk_add_f32 v[8:9], v[8:9], v[138:139]
	v_fmac_f32_e32 v130, v12, v12
	v_fmac_f32_e32 v131, v14, v14
	v_pk_add_f32 v[2:3], v[2:3], v[132:133]
	v_add_f32_e32 v130, v130, v131
	v_mul_f32_e32 v131, v9, v9
	v_mul_f32_e32 v132, v11, v11
	v_fmac_f32_e32 v131, v8, v8
	v_fmac_f32_e32 v132, v10, v10
	v_pk_add_f32 v[6:7], v[6:7], v[136:137]
	v_pk_add_f32 v[4:5], v[4:5], v[134:135]
	v_add_f32_e32 v131, v131, v132
	v_add_f32_e32 v130, v130, v131
	v_mul_f32_e32 v131, v5, v5
	v_mul_f32_e32 v132, v7, v7
	v_fmac_f32_e32 v131, v4, v4
	v_fmac_f32_e32 v132, v6, v6
	v_add_f32_e32 v131, v131, v132
	v_add_f32_e32 v130, v130, v131
	v_mul_f32_e32 v131, v1, v1
	v_mul_f32_e32 v132, v3, v3
	v_fmac_f32_e32 v131, v0, v0
	v_fmac_f32_e32 v132, v2, v2
	v_add_f32_e32 v131, v131, v132
	v_add_f32_e32 v130, v130, v131
	ds_swizzle_b32 v131, v130 offset:swizzle(SWAP,16)
	s_waitcnt lgkmcnt(0)
	v_add_f32_e32 v130, v130, v131
	v_mov_b32_e32 v131, v130
	s_nop 1
	v_permlane32_swap_b32_e32 v130, v131
	s_and_saveexec_b64 s[0:1], vcc
	s_lshl_b32 s19, s19, 10
	s_add_i32 s20, s20, s19
	v_lshl_add_u32 v132, v247, 4, s20
	v_add_f32_e32 v130, v130, v131
	ds_write_b32 v132, v130 offset:2816
	s_or_b64 exec, exec, s[0:1]
	v_and_b32_e32 v130, 31, v251
	s_waitcnt lgkmcnt(0)
	s_barrier
	v_lshl_or_b32 v132, s3, 5, v130
	v_add_u32_e32 v130, s10, v132
	v_cmp_gt_u32_e64 s[0:1], 32, v96
	v_ashrrev_i32_e32 v131, 31, v130
	s_and_saveexec_b64 s[20:21], s[0:1]
	s_cbranch_execz .LBB0_249
	v_lshl_add_u32 v133, v132, 4, 0
	ds_read_b128 v[134:137], v133
	v_readlane_b32 s34, v253, 29
	v_readlane_b32 s35, v253, 30
	s_ashr_i32 s3, s2, 31
	s_waitcnt lgkmcnt(0)
	v_mov_b32_e32 v138, v135
	v_mov_b32_e32 v139, v136
	v_mov_b32_e32 v135, v137
	v_pk_add_f32 v[134:135], v[138:139], v[134:135]
	v_lshl_add_u64 v[136:137], v[130:131], 4, s[34:35]
	v_pk_add_f32 v[134:135], v[134:135], v[134:135] op_sel:[0,1] op_sel_hi:[1,0]
	v_lshl_add_u64 v[136:137], s[2:3], 2, v[136:137]
	global_store_dword v[136:137], v134, off sc1
